# prologue role split (grid 256): 64 CUs (8 per XCD) run the latency-bound helper steps (Fourier-weight fold, memory K/V) while 192 CUs stream the weight transposes
# speedup vs baseline: 1.0155x; 1.0155x over previous
.LBB0_14:
	s_mov_b32 s99, s43
	s_mov_b32 s98, s42
	s_cmp_lg_u32 s42, 0x100
	s_cbranch_scc1 .Lp0_go
	s_and_b32 s98, s43, 31
	s_lshr_b32 s99, s43, 5
	s_cmp_lt_u32 s98, 8
	s_cbranch_scc1 .Lp0_roleB
	s_mul_i32 s99, s99, 24
	s_add_i32 s99, s99, s98
	s_add_i32 s99, s99, -8
	s_movk_i32 s98, 0xc0
	s_branch .Lp0_go
.Lp0_roleB:
	s_movk_i32 s99, 0x4000
	s_movk_i32 s98, 0xc0
.Lp0_go:
	s_lshl_b32 s0, s99, 3
	s_add_i32 s8, s0, s91
	s_mov_b32 s0, 24
	s_ashr_i32 s1, s0, 31
	s_lshl_b32 s10, s98, 3
	s_lshl_b64 s[0:1], s[0:1], 3
	s_add_u32 s0, s92, s0
	s_addc_u32 s1, s93, s1
	s_load_dwordx2 s[6:7], s[0:1], 0x0
	s_cmp_gt_i32 s8, 0xaf7f
	v_mbcnt_lo_u32_b32 v0, -1, 0
	v_mbcnt_hi_u32_b32 v0, -1, v0
	s_cbranch_scc1 .LBB0_898
	s_mul_i32 s0, s91, 0x2100
	s_add_i32 s0, s0, 0
	v_lshlrev_b32_e32 v1, 2, v0
	s_waitcnt lgkmcnt(0)
	s_add_u32 s14, s6, 0x17000000
	v_bfe_u32 v136, v0, 3, 3
	v_and_b32_e32 v2, 28, v1
	s_movk_i32 s1, 0x84
	v_mov_b32_e32 v1, 0x420
	s_addc_u32 s15, s7, 0
	v_mad_u32_u24 v147, v136, s1, v1
	v_mov_b32_e32 v1, 0xc60
	s_add_u32 s9, s6, 0x6e00000
	v_mad_u32_u24 v151, v136, s1, v1
	v_mov_b32_e32 v1, 0x14a0
	s_addc_u32 s11, s7, 0
	v_mad_u32_u24 v153, v136, s1, v1
	v_mov_b32_e32 v1, 0x18c0
	s_add_u32 s17, s6, 0x5a00000
	v_lshl_add_u32 v144, v2, 2, s0
	v_mad_u32_u24 v1, v136, s1, v1
	s_addc_u32 s44, s7, 0
	v_add_u32_e32 v154, v144, v1
	v_lshlrev_b32_e32 v1, 3, v0
	s_add_u32 s45, s6, 0xa00000
	v_and_b32_e32 v140, 56, v1
	s_addc_u32 s46, s7, 0
	v_or_b32_e32 v146, 8, v136
	v_or_b32_e32 v148, 16, v136
	v_or_b32_e32 v150, 24, v136
	v_mul_u32_u24_e32 v1, 0x84, v140
	v_lshlrev_b32_e32 v4, 2, v136
	s_add_u32 s47, s6, 0x4e00000
	v_mad_u32_u24 v145, v136, s1, v144
	v_bfe_u32 v3, v0, 3, 2
	v_add3_u32 v155, s0, v1, v4
	v_lshrrev_b32_e32 v0, 2, v0
	v_lshlrev_b32_e32 v1, 1, v146
	v_lshlrev_b32_e32 v4, 1, v148
	v_lshlrev_b32_e32 v5, 1, v150
	s_addc_u32 s48, s7, 0
	s_lshl_b32 s0, s99, 5
	s_lshl_b32 s1, s91, 2
	v_mov_b32_e32 v139, 0
	s_movk_i32 s2, 0x420
	v_and_b32_e32 v0, 8, v0
	v_and_b32_e32 v1, 24, v1
	v_and_b32_e32 v4, 40, v4
	v_and_b32_e32 v5, 56, v5
	s_add_i32 s1, s1, s0
	s_mov_b32 s5, 0
	v_add3_u32 v149, v147, v144, s2
	v_add3_u32 v152, v151, v144, s2
	v_mov_b32_e32 v141, v139
	v_or_b32_e32 v156, v0, v3
	v_or_b32_e32 v157, v1, v3
	v_or_b32_e32 v158, v4, v3
	v_or_b32_e32 v159, v5, v3
	v_or3_b32 v160, v136, v0, 4
	v_or3_b32 v161, v136, v1, 4
	v_or3_b32 v162, v136, v4, 4
	v_or3_b32 v163, v136, v5, 4
	v_mov_b32_e32 v137, v139
	s_sub_i32 s49, 0, s1
	s_lshl_b32 s50, s98, 5
	s_sub_i32 s51, 0x251fc, s1
	v_lshlrev_b32_e32 v142, 2, v2
	v_mov_b32_e32 v143, v139
	v_mov_b32_e32 v164, 0xffffff40
	s_movk_i32 s52, 0x200
	s_movk_i32 s53, 0xa00
	s_movk_i32 s54, 0xf600
	s_mov_b32 s16, 0x42800000
	v_mov_b32_e32 v165, 0x400
	v_mov_b32_e32 v166, 0xfffffa00
	v_mov_b32_e32 v167, 0xfffffe00
	s_mov_b32 s55, s8
	s_branch .LBB0_18

.LBB0_898:
	s_lshl_b32 s8, s43, 3
	s_add_i32 s8, s8, s91
	s_lshl_b32 s10, s42, 3
	s_lshl_b32 s22, s43, 9
	s_waitcnt lgkmcnt(0)
	s_barrier
	s_waitcnt vmcnt(0)
	v_mbcnt_lo_u32_b32 v0, -1, 0
	v_mbcnt_hi_u32_b32 v0, -1, v0
	s_add_i32 s0, s22, s41
	v_add_u32_e32 v0, s0, v0
	s_movk_i32 s1, 0x4000
	s_lshl_b32 s0, s42, 9
	v_cmp_gt_i32_e32 vcc, s1, v0
	v_ashrrev_i32_e32 v1, 31, v0
	s_and_saveexec_b64 s[2:3], vcc
	s_cbranch_execz .LBB0_903
	v_lshl_add_u64 v[2:3], v[0:1], 1, s[6:7]
	s_mov_b64 s[4:5], 0x100000
	s_ashr_i32 s1, s0, 31
	v_lshl_add_u64 v[2:3], v[2:3], 0, s[4:5]
	s_lshl_b64 s[14:15], s[0:1], 1
	s_mov_b64 s[4:5], 0
	s_mov_b32 s1, 0x7f800000
	v_mov_b32_e32 v4, 0xbf1f24be
	v_mov_b32_e32 v5, 0x3e642e9d
	v_mov_b32_e32 v6, 0x7fc00000
	s_movk_i32 s9, 0x7fff
	s_brev_b32 s11, 1
	s_movk_i32 s16, 0x3fff
	v_mov_b32_e32 v7, v0

.LBB0_913:
	s_cmp_lg_u32 s42, 0x100
	s_cbranch_scc1 .Lp0_noremap
	s_and_b32 s98, s43, 31
	s_lshr_b32 s99, s43, 5
	s_cmp_lt_u32 s98, 8
	s_cbranch_scc1 .Lp0_foldB
	s_movk_i32 s43, 0x100
	s_branch .Lp0_foldset
.Lp0_foldB:
	s_mul_i32 s99, s99, 8
	s_add_i32 s43, s99, s98
.Lp0_foldset:
	s_movk_i32 s42, 64
	s_lshl_b32 s22, s43, 9
	s_lshl_b32 s0, s42, 9
